# expert-weight conversion partly hidden inside attention unit 1 (LDS-DMA half-tiles into spare LDS, converted next iteration with the 12 free VGPRs), burst shrunk to the rest; quotas 164/228
# speedup vs baseline: 1.0154x; 1.0154x over previous
.Lconv_entry:
	v_readlane_b32 s0, v255, 7
	s_and_b32 s1, s76, 31
	s_lshl_b32 s1, s1, 3
	s_lshr_b32 s2, s76, 5
	s_or_b32 s1, s1, s2
	s_mul_i32 s2, s1, 0xa4
	s_sub_u32 s3, s1, 0x90
	s_mul_i32 s3, s3, 0xe4
	s_add_u32 s3, s3, 0x5c40
	s_movk_i32 s15, 0xe4
	s_cmp_lt_u32 s1, 0x90
	s_cselect_b32 s14, s2, s3
	s_cselect_b32 s15, 0xa4, s15
	s_add_u32 s15, s15, s14
	s_add_u32 s14, s14, s0
	s_add_u32 s14, s14, 0x80
	v_lshrrev_b32_e32 v2, 3, v254
	v_lshlrev_b32_e32 v2, 4, v2
	v_and_b32_e32 v3, 7, v254
	v_lshlrev_b32_e32 v4, 4, v3
	v_lshlrev_b32_e32 v3, 2, v3
	v_mov_b32_e32 v5, 0x43e00000
	s_mov_b32 s25, 0xc3e00000
	s_cmp_lt_u32 s14, s15
	s_cbranch_scc0 .Lconv_done
	s_cmp_lt_u32 s14, 0x8000
	s_cbranch_scc0 .Lconv_dn_p
	s_lshr_b32 s0, s14, 14
	s_and_b32 s1, s14, 0x3fff
	s_cmp_eq_u32 s0, 0
	s_cselect_b32 s16, s36, s38
	s_cselect_b32 s17, s37, s39
	s_lshr_b32 s2, s1, 8
	s_and_b32 s3, s1, 0xff
	s_lshr_b32 s1, s3, 4
	s_and_b32 s3, s3, 15
	s_lshl_b32 s10, s2, 22
	s_lshl_b32 s11, s1, 18
	s_add_u32 s10, s10, s11
	s_lshl_b32 s11, s3, 7
	s_add_u32 s10, s10, s11
	s_add_u32 s16, s16, s10
	s_addc_u32 s17, s17, 0
	s_movk_i32 s18, 0x800
	s_lshl_b32 s10, s2, 10
	s_lshr_b32 s11, s3, 2
	s_lshl_b32 s11, s11, 8
	s_add_u32 s10, s10, s11
	s_lshl_b32 s11, s0, 7
	s_add_u32 s10, s10, s11
	s_and_b32 s11, s3, 3
	s_lshl_b32 s11, s11, 5
	s_add_u32 s10, s10, s11
	s_lshl_b32 s10, s10, 11
	s_lshl_b32 s11, s1, 7
	s_add_u32 s10, s10, s11
	s_add_u32 s20, s50, 0x1c200000
	s_addc_u32 s21, s51, 0
	s_add_u32 s20, s20, s10
	s_addc_u32 s21, s21, 0
	s_movk_i32 s19, 0x800
	s_branch .Lconv_ad_p

.LBB0_1140:
	s_bfe_u32 s2, s76, 0x10007
	s_lshl_b32 s1, s76, 19
	s_lshl_b32 s10, s76, 3
	s_bfe_u32 s3, s76, 0x20005
	s_lshl_b32 s0, s2, 23
	s_and_b32 s1, s1, 0x780000
	s_and_b32 s10, s10, 0x80
	s_and_b32 s11, s76, 0xffffff00
	s_or_b32 s0, s0, s1
	s_lshl_b32 s1, s3, 9
	s_or_b32 s10, s10, s11
	s_add_i32 s10, s10, s1
	s_ashr_i32 s1, s10, 31
	s_add_u32 s10, s0, s10
	s_addc_u32 s11, 0, s1
	s_lshl_b64 s[0:1], s[10:11], 1
	s_add_u32 s14, s8, s0
	s_addc_u32 s15, s9, s1
	s_mul_i32 s2, s2, 0x440000
	s_lshl_b32 s0, s3, 8
	s_or_b32 s34, s0, s2
	s_add_u32 s0, s42, s34
	s_addc_u32 s1, s43, 0
	v_and_b32_e32 v1, 0x78, v192
	s_add_u32 s2, s54, s34
	v_lshlrev_b32_e32 v1, 1, v1
	s_waitcnt vmcnt(18) lgkmcnt(9)
	v_or_b32_e32 v20, 32, v194
	s_addc_u32 s3, s55, 0
	v_lshl_or_b32 v67, v194, 10, v1
	s_waitcnt lgkmcnt(5)
	v_lshl_or_b32 v14, v20, 10, v1
	global_load_dwordx4 v[2:5], v67, s[2:3]
	global_load_dwordx4 v[6:9], v14, s[2:3]
	global_load_dwordx4 v[10:13], v67, s[0:1]
	s_waitcnt lgkmcnt(2)
	global_load_dwordx4 v[14:17], v14, s[0:1]
	v_lshrrev_b32_e32 v181, 6, v0
	v_and_b32_e32 v179, 31, v0
	v_lshlrev_b32_e32 v18, 17, v181
	v_lshrrev_b32_e32 v193, 5, v254
	v_lshl_or_b32 v182, v179, 12, v18
	v_mov_b32_e32 v183, 0
	v_lshl_add_u64 v[18:19], s[14:15], 0, v[182:183]
	v_lshlrev_b32_e32 v182, 4, v193
	v_lshl_add_u64 v[18:19], v[18:19], 0, v[182:183]
	global_load_dwordx4 v[126:129], v[18:19], off nt
	global_load_dwordx4 v[114:117], v[18:19], off offset:32 nt
	global_load_dwordx4 v[118:121], v[18:19], off offset:64 nt
	global_load_dwordx4 v[122:125], v[18:19], off offset:96 nt
	global_load_dwordx4 v[110:113], v[18:19], off offset:128 nt
	global_load_dwordx4 v[106:109], v[18:19], off offset:160 nt
	global_load_dwordx4 v[102:105], v[18:19], off offset:192 nt
	global_load_dwordx4 v[98:101], v[18:19], off offset:224 nt
	v_lshrrev_b32_e32 v21, 3, v0
	v_and_b32_e32 v21, 8, v21
	s_waitcnt vmcnt(29)
	v_lshlrev_b32_e32 v24, 8, v194
	v_and_b32_e32 v25, 0x70, v0
	s_waitcnt vmcnt(28) lgkmcnt(0)
	v_lshlrev_b32_e32 v27, 8, v20
	v_and_or_b32 v29, v194, 16, v21
	v_lshrrev_b32_e32 v22, 5, v0
	v_bfe_u32 v23, v192, 5, 2
	v_and_b32_e32 v30, 48, v1
	v_and_or_b32 v20, v20, 48, v21
	v_bitop3_b32 v21, v1, v24, v25 bitop3:0xde
	v_bitop3_b32 v1, v1, v27, v25 bitop3:0xde
	v_lshrrev_b32_e32 v24, 1, v29
	v_and_or_b32 v22, v22, 4, v195
	v_add_u32_e32 v202, 0, v1
	v_or_b32_e32 v1, v24, v23
	v_lshlrev_b32_e32 v26, 4, v0
	v_lshlrev_b32_e32 v22, 6, v22
	v_lshrrev_b32_e32 v20, 1, v20
	v_lshlrev_b32_e32 v1, 9, v1
	v_lshlrev_b32_e32 v28, 8, v179
	v_and_b32_e32 v178, 0x70, v26
	v_or_b32_e32 v20, v20, v23
	v_or3_b32 v1, v1, v22, v30
	v_lshlrev_b32_e32 v20, 9, v20
	v_add_u32_e32 v203, 0, v1
	v_bitop3_b32 v1, v182, v28, v178 bitop3:0xde
	v_or3_b32 v20, v20, v22, v30
	v_add_u32_e32 v205, 0, v1
	v_add_u32_e32 v201, 0, v21
	v_add_u32_e32 v204, 0, v20
	s_waitcnt vmcnt(0)
	v_or_b32_e32 v1, 32, v182
	v_bitop3_b32 v1, v1, v28, v178 bitop3:0xde
	v_add_u32_e32 v206, 0, v1
	v_or_b32_e32 v1, 64, v182
	v_bitop3_b32 v1, v1, v28, v178 bitop3:0xde
	v_add_u32_e32 v207, 0, v1
	v_or_b32_e32 v1, 0x60, v182
	v_bitop3_b32 v1, v1, v28, v178 bitop3:0xde
	v_add_u32_e32 v208, 0, v1
	v_or_b32_e32 v1, 0x80, v182
	v_bitop3_b32 v1, v1, v28, v178 bitop3:0xde
	v_add_u32_e32 v209, 0, v1
	v_or_b32_e32 v1, 0xa0, v182
	v_bitop3_b32 v1, v1, v28, v178 bitop3:0xde
	v_add_u32_e32 v210, 0, v1
	v_lshlrev_b32_e32 v27, 1, v0
	v_and_b32_e32 v29, 0x118, v192
	v_and_b32_e32 v26, 0xc0, v26
	s_waitcnt vmcnt(11)
	ds_write_b128 v203, v[2:5]
	s_waitcnt vmcnt(10)
	ds_write_b128 v204, v[6:9]
	s_waitcnt vmcnt(9)
	ds_write_b128 v201, v[10:13] offset:32768
	s_waitcnt vmcnt(8)
	ds_write_b128 v202, v[14:17] offset:32768
	s_waitcnt lgkmcnt(0)
	s_barrier
	ds_read_b128 v[2:5], v205 offset:32768
	ds_read_b128 v[6:9], v205 offset:40960
	s_waitcnt vmcnt(7) lgkmcnt(1)
	v_mfma_f32_32x32x16_bf16 v[34:49], v[2:5], v[126:129], 0
	ds_read_b128 v[18:21], v206 offset:32768
	ds_read_b128 v[22:25], v206 offset:40960
	v_and_b32_e32 v27, 32, v27
	v_and_b32_e32 v1, 0x1c0, v0
	v_or3_b32 v68, v27, v26, v29
	v_or_b32_e32 v26, 0xe0, v182
	s_add_i32 s14, 0, 0x10000
	v_lshl_add_u32 v196, v1, 2, s14
	s_waitcnt lgkmcnt(2)
	v_mfma_f32_32x32x16_bf16 v[2:17], v[6:9], v[126:129], 0
	v_bitop3_b32 v1, v26, v28, v178 bitop3:0xde
	v_add_u32_e32 v212, 0, v1
	s_mov_b32 s16, 0
	s_mov_b32 s30, s16
	s_mov_b32 s31, s16
	s_mov_b32 s17, s16
	s_mov_b32 s18, s16
	s_waitcnt vmcnt(6) lgkmcnt(1)
	v_mfma_f32_32x32x16_bf16 v[34:49], v[18:21], v[114:117], v[34:49]
	s_mov_b32 s19, s16
	s_mov_b32 s20, s16
	s_mov_b32 s21, s16
	s_mov_b32 s22, s16
	s_mov_b32 s23, s16
	s_mov_b32 s24, s16
	s_mov_b32 s25, s16
	s_waitcnt lgkmcnt(0)
	v_mfma_f32_32x32x16_bf16 v[2:17], v[22:25], v[114:117], v[2:17]
	ds_read_b128 v[18:21], v207 offset:32768
	ds_read_b128 v[22:25], v207 offset:40960
	s_mov_b32 s26, s16
	s_mov_b32 s27, s16
	s_mov_b32 s28, s16
	s_mov_b32 s29, s16
	v_or_b32_e32 v58, 0x10000, v67
	v_or_b32_e32 v62, 0x18000, v67
	s_waitcnt vmcnt(5) lgkmcnt(1)
	v_mfma_f32_32x32x16_bf16 v[34:49], v[18:21], v[118:121], v[34:49]
	v_or_b32_e32 v69, 0x20000, v67
	s_cmp_lg_u32 0, -1
	s_cselect_b32 s35, 0, 0
	s_mov_b32 s15, 1
	v_add_u32_e32 v199, s35, v68
	s_mov_b32 s14, 0x3e0293ee
	v_lshlrev_b32_e32 v180, 16, v181
	s_waitcnt lgkmcnt(0)
	v_mfma_f32_32x32x16_bf16 v[2:17], v[22:25], v[118:121], v[2:17]
	ds_read_b128 v[18:21], v208 offset:32768
	ds_read_b128 v[22:25], v208 offset:40960
	v_lshl_add_u32 v197, v179, 2, v196
	v_or_b32_e32 v184, 0x48000, v67
	v_mov_b32_e32 v185, v183
	v_or_b32_e32 v186, 0x40000, v67
	v_mov_b32_e32 v187, v183
	v_or_b32_e32 v188, 0x30000, v67
	s_waitcnt vmcnt(4) lgkmcnt(1)
	v_mfma_f32_32x32x16_bf16 v[34:49], v[18:21], v[122:125], v[34:49]
	v_mov_b32_e32 v189, v183
	v_or_b32_e32 v190, 0x38000, v67
	v_mov_b32_e32 v191, v183
	s_waitcnt lgkmcnt(0)
	v_mfma_f32_32x32x16_bf16 v[2:17], v[22:25], v[122:125], v[2:17]
	ds_read_b128 v[18:21], v209 offset:32768
	ds_read_b128 v[22:25], v209 offset:40960
	ds_read_b128 v[50:53], v212 offset:40960
	s_waitcnt vmcnt(3) lgkmcnt(2)
	v_mfma_f32_32x32x16_bf16 v[34:49], v[18:21], v[110:113], v[34:49]
	ds_read_b128 v[18:21], v210 offset:32768
	s_waitcnt lgkmcnt(2)
	v_mfma_f32_32x32x16_bf16 v[2:17], v[22:25], v[110:113], v[2:17]
	ds_read_b128 v[22:25], v210 offset:40960
	s_waitcnt vmcnt(2) lgkmcnt(1)
	v_mfma_f32_32x32x16_bf16 v[34:49], v[18:21], v[106:109], v[34:49]
	v_or_b32_e32 v18, 0xc0, v182
	v_bitop3_b32 v18, v18, v28, v178 bitop3:0xde
	v_add_u32_e32 v211, 0, v18
	ds_read_b128 v[18:21], v211 offset:32768
	s_waitcnt lgkmcnt(1)
	v_mfma_f32_32x32x16_bf16 v[2:17], v[22:25], v[106:109], v[2:17]
	ds_read_b128 v[22:25], v211 offset:40960
	s_waitcnt vmcnt(1) lgkmcnt(1)
	v_mfma_f32_32x32x16_bf16 v[34:49], v[18:21], v[102:105], v[34:49]
	ds_read_b128 v[18:21], v212 offset:32768
	s_waitcnt lgkmcnt(1)
	v_mfma_f32_32x32x16_bf16 v[2:17], v[22:25], v[102:105], v[2:17]
	s_waitcnt vmcnt(0) lgkmcnt(0)
	v_mfma_f32_32x32x16_bf16 v[34:49], v[18:21], v[98:101], v[34:49]
	v_mov_b64_e32 v[32:33], s[30:31]
	v_mov_b64_e32 v[30:31], s[28:29]
	v_mov_b64_e32 v[28:29], s[26:27]
	v_mov_b64_e32 v[26:27], s[24:25]
	v_mov_b64_e32 v[24:25], s[22:23]
	v_mov_b64_e32 v[22:23], s[20:21]
	v_mov_b64_e32 v[20:21], s[18:19]
	v_mfma_f32_32x32x16_bf16 v[2:17], v[50:53], v[98:101], v[2:17]
	s_nop 3
	v_max_f32_e32 v1, v35, v35
	v_max_f32_e32 v50, v34, v34
	v_max_f32_e32 v1, v50, v1
	v_max3_f32 v1, v1, v36, v37
	v_max3_f32 v1, v1, v38, v39
	v_max3_f32 v1, v1, v40, v41
	v_max3_f32 v1, v1, v42, v43
	v_max3_f32 v1, v1, v44, v45
	v_max3_f32 v1, v1, v46, v47
	v_max3_f32 v1, v1, v48, v49
	v_max3_f32 v1, v1, v2, v3
	v_max3_f32 v1, v1, v4, v5
	v_max3_f32 v1, v1, v6, v7
	v_max3_f32 v1, v1, v8, v9
	v_max3_f32 v1, v1, v10, v11
	v_max3_f32 v1, v1, v12, v13
	v_max3_f32 v1, v1, v14, v15
	v_max3_f32 v1, v1, v16, v17
	v_mov_b32_e32 v66, v1
	s_nop 1
	v_permlane32_swap_b32_e32 v1, v66
	v_max_f32_e32 v66, v66, v66
	v_max_f32_e32 v1, v1, v1
	v_max_f32_e32 v1, v1, v66
	v_mov_b64_e32 v[18:19], s[16:17]
	v_add_f32_e32 v66, 0x7149f2ca, v1
	s_mov_b32 s22, 0x42b504f3
	v_cmp_ge_f32_e32 vcc, s22, v66
	v_or_b32_e32 v66, 0x28000, v67
	global_load_dwordx4 v[50:53], v58, s[2:3]
	global_load_dwordx4 v[54:57], v62, s[2:3]
	s_nop 0
	global_load_dwordx4 v[58:61], v58, s[0:1]
	s_nop 0
	global_load_dwordx4 v[62:65], v62, s[0:1]
	s_nop 0
	global_load_dwordx4 v[142:145], v66, s[0:1]
	global_load_dwordx4 v[134:137], v66, s[2:3]
	global_load_dwordx4 v[138:141], v69, s[0:1]
	global_load_dwordx4 v[130:133], v69, s[2:3]
	v_max_f32_e32 v1, 0xf149f2ca, v1
	v_sub_f32_e32 v66, 0xf149f2ca, v1
	v_mul_f32_e32 v66, 0x3e0293ee, v66
	v_exp_f32_e32 v66, v66
	s_cmp_eq_u64 vcc, exec
	v_mov_b32_e32 v69, 0xf149f2ca
	s_cselect_b64 vcc, -1, 0
	v_cndmask_b32_e32 v166, v1, v69, vcc
	v_cndmask_b32_e64 v213, v66, 1.0, vcc
	v_mul_f32_e32 v66, 0xbe0293ee, v166
	v_fmamk_f32 v1, v34, 0x3e0293ee, v66
	v_fmamk_f32 v34, v35, 0x3e0293ee, v66
	v_fmamk_f32 v35, v36, 0x3e0293ee, v66
	v_fmamk_f32 v36, v37, 0x3e0293ee, v66
	v_fmamk_f32 v37, v38, 0x3e0293ee, v66
	v_fmamk_f32 v38, v39, 0x3e0293ee, v66
	v_fmamk_f32 v39, v40, 0x3e0293ee, v66
	v_fmamk_f32 v40, v41, 0x3e0293ee, v66
	v_fmamk_f32 v41, v42, 0x3e0293ee, v66
	v_fmamk_f32 v42, v43, 0x3e0293ee, v66
	v_fmamk_f32 v43, v44, 0x3e0293ee, v66
	v_fmamk_f32 v44, v45, 0x3e0293ee, v66
	v_fmamk_f32 v45, v46, 0x3e0293ee, v66
	v_fmamk_f32 v46, v47, 0x3e0293ee, v66
	v_fmamk_f32 v47, v48, 0x3e0293ee, v66
	v_mov_b32_e32 v48, v66
	v_fmac_f32_e32 v48, 0x3e0293ee, v49
	v_exp_f32_e32 v177, v1
	v_exp_f32_e32 v220, v34
	v_exp_f32_e32 v163, v35
	v_exp_f32_e32 v217, v36
	v_exp_f32_e32 v164, v37
	v_exp_f32_e32 v176, v38
	v_exp_f32_e32 v165, v39
	v_exp_f32_e32 v175, v40
	v_exp_f32_e32 v172, v41
	v_exp_f32_e32 v174, v42
	v_exp_f32_e32 v171, v43
	v_exp_f32_e32 v173, v44
	v_exp_f32_e32 v168, v45
	v_exp_f32_e32 v170, v46
	v_exp_f32_e32 v167, v47
	v_exp_f32_e32 v169, v48
	s_waitcnt vmcnt(4)
	s_addk_i32 s35, 0x4000
	v_pk_fma_f32 v[152:153], v[16:17], s[14:15], v[66:67] op_sel_hi:[1,0,0]
	v_pk_fma_f32 v[158:159], v[14:15], s[14:15], v[66:67] op_sel_hi:[1,0,0]
	v_pk_fma_f32 v[160:161], v[12:13], s[14:15], v[66:67] op_sel_hi:[1,0,0]
	v_pk_fma_f32 v[146:147], v[10:11], s[14:15], v[66:67] op_sel_hi:[1,0,0]
	v_pk_fma_f32 v[148:149], v[8:9], s[14:15], v[66:67] op_sel_hi:[1,0,0]
	v_pk_fma_f32 v[150:151], v[6:7], s[14:15], v[66:67] op_sel_hi:[1,0,0]
	v_pk_fma_f32 v[154:155], v[4:5], s[14:15], v[66:67] op_sel_hi:[1,0,0]
	v_pk_fma_f32 v[156:157], v[2:3], s[14:15], v[66:67] op_sel_hi:[1,0,0]
	s_waitcnt vmcnt(7)
	ds_write_b128 v203, v[50:53] offset:16384
	s_waitcnt vmcnt(6)
	ds_write_b128 v204, v[54:57] offset:16384
	s_waitcnt vmcnt(5)
	ds_write_b128 v201, v[58:61] offset:49152
	s_waitcnt vmcnt(4)
	ds_write_b128 v202, v[62:65] offset:49152
	s_add_u32 s16, s50, s34
	v_mov_b64_e32 v[64:65], v[32:33]
	v_mov_b64_e32 v[48:49], v[32:33]
	v_mov_b64_e32 v[2:3], v[18:19]
	v_cmp_gt_u32_e64 s[0:1], 32, v254
	v_add_u32_e32 v198, s35, v68
	s_addc_u32 s17, s51, 0
	s_mov_b32 s23, 0x5f00000
	s_mov_b32 s24, 0x5600000
	v_mov_b64_e32 v[62:63], v[30:31]
	v_mov_b64_e32 v[60:61], v[28:29]
	v_mov_b64_e32 v[58:59], v[26:27]
	v_mov_b64_e32 v[56:57], v[24:25]
	v_mov_b64_e32 v[54:55], v[22:23]
	v_mov_b64_e32 v[52:53], v[20:21]
	v_mov_b64_e32 v[50:51], v[18:19]
	v_mov_b64_e32 v[46:47], v[30:31]
	v_mov_b64_e32 v[44:45], v[28:29]
	v_mov_b64_e32 v[42:43], v[26:27]
	v_mov_b64_e32 v[40:41], v[24:25]
	v_mov_b64_e32 v[38:39], v[22:23]
	v_mov_b64_e32 v[36:37], v[20:21]
	v_mov_b64_e32 v[34:35], v[18:19]
	v_mov_b64_e32 v[4:5], v[20:21]
	v_mov_b64_e32 v[6:7], v[22:23]
	v_mov_b64_e32 v[8:9], v[24:25]
	v_mov_b64_e32 v[10:11], v[26:27]
	v_mov_b64_e32 v[12:13], v[28:29]
	v_mov_b64_e32 v[14:15], v[30:31]
	v_mov_b64_e32 v[16:17], v[32:33]
	s_waitcnt lgkmcnt(0)
	s_barrier
	v_readlane_b32 s90, v255, 7
	s_and_b32 s91, s76, 31
	s_lshl_b32 s91, s91, 3
	s_lshr_b32 s92, s76, 5
	s_or_b32 s91, s91, s92
	s_mul_i32 s92, s91, 0xa4
	s_sub_u32 s93, s91, 0x90
	s_mul_i32 s93, s93, 0xe4
	s_add_u32 s93, s93, 0x5c40
	s_movk_i32 s78, 0xe4
	s_cmp_lt_u32 s91, 0x90
	s_cselect_b32 s77, s92, s93
	s_cselect_b32 s78, 0xa4, s78
	s_add_u32 s78, s78, s77
	s_add_u32 s77, s77, s90
	s_lshl_b32 s87, s90, 13
	s_add_u32 s87, s87, 0x10800
	s_lshl_b32 s88, s90, 11
	s_add_u32 s88, s88, 0x24000
	s_mov_b32 s79, 0
	s_mov_b32 s89, 0
.LBB0_1141:
	ds_read_b128 v[66:69], v205 offset:49152
	ds_read_b128 v[70:73], v205 offset:57344
	ds_read_b128 v[222:225], v206 offset:49152
	ds_read_b128 v[226:229], v206 offset:57344
	v_exp_f32_e32 v1, v156
	v_exp_f32_e32 v156, v157
	s_waitcnt lgkmcnt(3)
	v_mfma_f32_32x32x16_bf16 v[82:97], v[66:69], v[126:129], 0
	v_exp_f32_e32 v157, v160
	v_exp_f32_e32 v160, v161
	v_add_f32_e32 v161, 0, v177
	v_add_f32_e32 v161, v220, v161
	v_add_f32_e32 v161, v163, v161
	v_add_f32_e32 v161, v217, v161
	v_add_f32_e32 v161, v164, v161
	s_waitcnt lgkmcnt(2)
	v_mfma_f32_32x32x16_bf16 v[66:81], v[70:73], v[126:129], 0
	v_add_f32_e32 v161, v176, v161
	v_add_f32_e32 v161, v165, v161
	v_add_f32_e32 v161, v175, v161
	v_add_f32_e32 v161, v172, v161
	v_add_f32_e32 v161, v174, v161
	v_add_f32_e32 v161, v171, v161
	v_add_f32_e32 v161, v173, v161
	s_waitcnt lgkmcnt(1)
	v_mfma_f32_32x32x16_bf16 v[82:97], v[222:225], v[114:117], v[82:97]
	v_add_f32_e32 v161, v168, v161
	v_add_f32_e32 v161, v170, v161
	v_exp_f32_e32 v154, v154
	v_add_f32_e32 v161, v167, v161
	v_exp_f32_e32 v155, v155
	v_add_f32_e32 v161, v169, v161
	v_exp_f32_e32 v150, v150
	s_waitcnt lgkmcnt(0)
	v_mfma_f32_32x32x16_bf16 v[66:81], v[226:229], v[114:117], v[66:81]
	ds_read_b128 v[222:225], v207 offset:49152
	ds_read_b128 v[226:229], v207 offset:57344
	v_add_f32_e32 v161, v1, v161
	v_exp_f32_e32 v151, v151
	v_add_f32_e32 v161, v156, v161
	v_exp_f32_e32 v148, v148
	v_add_f32_e32 v161, v154, v161
	v_exp_f32_e32 v149, v149
	s_waitcnt lgkmcnt(1)
	v_mfma_f32_32x32x16_bf16 v[82:97], v[222:225], v[118:121], v[82:97]
	v_add_f32_e32 v161, v155, v161
	v_exp_f32_e32 v146, v146
	v_add_f32_e32 v161, v150, v161
	v_exp_f32_e32 v147, v147
	v_add_f32_e32 v161, v151, v161
	v_add_f32_e32 v161, v148, v161
	v_add_f32_e32 v161, v149, v161
	s_waitcnt lgkmcnt(0)
	v_mfma_f32_32x32x16_bf16 v[66:81], v[226:229], v[118:121], v[66:81]
	ds_read_b128 v[222:225], v208 offset:49152
	ds_read_b128 v[226:229], v208 offset:57344
	v_exp_f32_e32 v158, v158
	v_add_f32_e32 v161, v146, v161
	v_exp_f32_e32 v159, v159
	v_add_f32_e32 v161, v147, v161
	v_exp_f32_e32 v152, v152
	v_add_f32_e32 v161, v157, v161
	s_waitcnt lgkmcnt(1)
	v_mfma_f32_32x32x16_bf16 v[82:97], v[222:225], v[122:125], v[82:97]
	v_exp_f32_e32 v153, v153
	v_add_f32_e32 v161, v160, v161
	v_add_f32_e32 v161, v158, v161
	v_add_f32_e32 v161, v159, v161
	v_add_f32_e32 v161, v152, v161
	v_add_f32_e32 v214, v153, v161
	v_mov_b32_e32 v215, v214
	s_waitcnt lgkmcnt(0)
	v_mfma_f32_32x32x16_bf16 v[66:81], v[226:229], v[122:125], v[66:81]
	ds_read_b128 v[222:225], v209 offset:49152
	ds_read_b128 v[226:229], v209 offset:57344
	v_permlane32_swap_b32_e32 v214, v215
	s_waitcnt lgkmcnt(1)
	v_mfma_f32_32x32x16_bf16 v[82:97], v[222:225], v[110:113], v[82:97]
	s_waitcnt lgkmcnt(0)
	v_mfma_f32_32x32x16_bf16 v[66:81], v[226:229], v[110:113], v[66:81]
	ds_read_b128 v[222:225], v210 offset:49152
	ds_read_b128 v[226:229], v210 offset:57344
	s_waitcnt lgkmcnt(1)
	v_mfma_f32_32x32x16_bf16 v[82:97], v[222:225], v[106:109], v[82:97]
	s_waitcnt lgkmcnt(0)
	v_mfma_f32_32x32x16_bf16 v[66:81], v[226:229], v[106:109], v[66:81]
	ds_read_b128 v[222:225], v211 offset:49152
	ds_read_b128 v[226:229], v211 offset:57344
	s_waitcnt lgkmcnt(1)
	v_mfma_f32_32x32x16_bf16 v[82:97], v[222:225], v[102:105], v[82:97]
	s_waitcnt lgkmcnt(0)
	v_mfma_f32_32x32x16_bf16 v[66:81], v[226:229], v[102:105], v[66:81]
	ds_read_b128 v[222:225], v212 offset:49152
	ds_read_b128 v[226:229], v212 offset:57344
	v_cvt_pk_bf16_f32 v162, v177, v220
	v_cvt_pk_bf16_f32 v163, v163, v217
	v_cvt_pk_bf16_f32 v164, v164, v176
	v_cvt_pk_bf16_f32 v165, v165, v175
	v_cvt_pk_bf16_f32 v172, v172, v174
	v_cvt_pk_bf16_f32 v173, v171, v173
	s_waitcnt lgkmcnt(1)
	v_mfma_f32_32x32x16_bf16 v[82:97], v[222:225], v[98:101], v[82:97]
	v_cvt_pk_bf16_f32 v174, v168, v170
	v_cvt_pk_bf16_f32 v175, v167, v169
	v_cvt_pk_bf16_f32 v168, v1, v156
	v_cvt_pk_bf16_f32 v169, v154, v155
	v_cvt_pk_bf16_f32 v170, v150, v151
	v_cvt_pk_bf16_f32 v171, v148, v149
	v_cvt_pk_bf16_f32 v216, v146, v147
	s_waitcnt lgkmcnt(0)
	v_mfma_f32_32x32x16_bf16 v[66:81], v[226:229], v[98:101], v[66:81]
	v_cvt_pk_bf16_f32 v217, v157, v160
	v_cvt_pk_bf16_f32 v218, v158, v159
	v_permlane32_swap_b32_e32 v162, v164
	v_cvt_pk_bf16_f32 v219, v152, v153
	v_permlane32_swap_b32_e32 v216, v218
	v_permlane32_swap_b32_e32 v163, v165
	v_permlane32_swap_b32_e32 v172, v174
	v_permlane32_swap_b32_e32 v173, v175
	v_permlane32_swap_b32_e32 v168, v170
	v_permlane32_swap_b32_e32 v169, v171
	v_permlane32_swap_b32_e32 v217, v219
	v_lshl_add_u64 v[154:155], s[16:17], 0, v[188:189]
	v_add_co_u32_e32 v146, vcc, s23, v154
	v_lshl_add_u64 v[156:157], s[16:17], 0, v[190:191]
	s_nop 0
	v_addc_co_u32_e32 v147, vcc, 0, v155, vcc
	v_add_co_u32_e32 v150, vcc, s23, v156
	s_nop 1
	v_addc_co_u32_e32 v151, vcc, 0, v157, vcc
	v_add_co_u32_e32 v154, vcc, s24, v154
	global_load_dwordx4 v[146:149], v[146:147], off
	s_nop 0
	global_load_dwordx4 v[150:153], v[150:151], off
	v_addc_co_u32_e32 v155, vcc, 0, v155, vcc
	v_add_co_u32_e32 v158, vcc, s24, v156
	s_nop 1
	v_addc_co_u32_e32 v159, vcc, 0, v157, vcc
	global_load_dwordx4 v[154:157], v[154:155], off
	s_nop 0
	global_load_dwordx4 v[158:161], v[158:159], off
	ds_read_b64_tr_b16 v[220:221], v199 offset:0
	ds_read_b64_tr_b16 v[222:223], v199 offset:0x800
	ds_read_b64_tr_b16 v[224:225], v199 offset:0x1000
	ds_read_b64_tr_b16 v[226:227], v199 offset:0x1800
	ds_read_b64_tr_b16 v[228:229], v199 offset:0x2000
	ds_read_b64_tr_b16 v[230:231], v199 offset:0x2800
	ds_read_b64_tr_b16 v[232:233], v199 offset:0x3000
	ds_read_b64_tr_b16 v[234:235], v199 offset:0x3800
	s_waitcnt lgkmcnt(0)
	s_nop 0
	v_mfma_f32_32x32x16_bf16 v[18:33], v[162:165], v[220:223], v[18:33]
	ds_read_b64_tr_b16 v[220:221], v199 offset:0x200
	ds_read_b64_tr_b16 v[222:223], v199 offset:0xa00
	v_mfma_f32_32x32x16_bf16 v[18:33], v[172:175], v[224:227], v[18:33]
	ds_read_b64_tr_b16 v[224:225], v199 offset:0x1200
	ds_read_b64_tr_b16 v[226:227], v199 offset:0x1a00
	v_mfma_f32_32x32x16_bf16 v[18:33], v[168:171], v[228:231], v[18:33]
	ds_read_b64_tr_b16 v[228:229], v199 offset:0x2200
	ds_read_b64_tr_b16 v[230:231], v199 offset:0x2a00
	ds_read_b64_tr_b16 v[236:237], v199 offset:0x3200
	ds_read_b64_tr_b16 v[238:239], v199 offset:0x3a00
	s_waitcnt lgkmcnt(0)
	v_mfma_f32_32x32x16_bf16 v[18:33], v[216:219], v[232:235], v[18:33]
	v_mfma_f32_32x32x16_bf16 v[50:65], v[162:165], v[220:223], v[50:65]
	ds_read_b64_tr_b16 v[220:221], v199 offset:0x400
	ds_read_b64_tr_b16 v[222:223], v199 offset:0xc00
	v_mfma_f32_32x32x16_bf16 v[50:65], v[172:175], v[224:227], v[50:65]
	ds_read_b64_tr_b16 v[224:225], v199 offset:0x1400
	ds_read_b64_tr_b16 v[226:227], v199 offset:0x1c00
	v_mfma_f32_32x32x16_bf16 v[50:65], v[168:171], v[228:231], v[50:65]
	ds_read_b64_tr_b16 v[228:229], v199 offset:0x2400
	ds_read_b64_tr_b16 v[230:231], v199 offset:0x2c00
	ds_read_b64_tr_b16 v[232:233], v199 offset:0x3400
	ds_read_b64_tr_b16 v[234:235], v199 offset:0x3c00
	s_waitcnt lgkmcnt(0)
	v_mfma_f32_32x32x16_bf16 v[50:65], v[216:219], v[236:239], v[50:65]
	v_mfma_f32_32x32x16_bf16 v[34:49], v[162:165], v[220:223], v[34:49]
	ds_read_b64_tr_b16 v[220:221], v199 offset:0x600
	ds_read_b64_tr_b16 v[222:223], v199 offset:0xe00
	v_mfma_f32_32x32x16_bf16 v[34:49], v[172:175], v[224:227], v[34:49]
	ds_read_b64_tr_b16 v[224:225], v199 offset:0x1600
	ds_read_b64_tr_b16 v[226:227], v199 offset:0x1e00
	v_mfma_f32_32x32x16_bf16 v[34:49], v[168:171], v[228:231], v[34:49]
	ds_read_b64_tr_b16 v[228:229], v199 offset:0x2600
	ds_read_b64_tr_b16 v[230:231], v199 offset:0x2e00
	ds_read_b64_tr_b16 v[236:237], v199 offset:0x3600
	ds_read_b64_tr_b16 v[238:239], v199 offset:0x3e00
	s_waitcnt lgkmcnt(0)
	v_mfma_f32_32x32x16_bf16 v[34:49], v[216:219], v[232:235], v[34:49]
	v_mfma_f32_32x32x16_bf16 v[2:17], v[162:165], v[220:223], v[2:17]
	v_max_f32_e32 v1, v83, v83
	v_max_f32_e32 v167, v82, v82
	v_max_f32_e32 v1, v167, v1
	v_max3_f32 v1, v1, v84, v85
	v_max3_f32 v1, v1, v86, v87
	v_max3_f32 v1, v1, v88, v89
	v_max3_f32 v1, v1, v90, v91
	v_max3_f32 v1, v1, v92, v93
	v_mfma_f32_32x32x16_bf16 v[2:17], v[172:175], v[224:227], v[2:17]
	v_max3_f32 v1, v1, v94, v95
	v_max3_f32 v1, v1, v96, v97
	v_max3_f32 v1, v1, v66, v67
	v_max3_f32 v1, v1, v68, v69
	v_max3_f32 v1, v1, v70, v71
	v_max3_f32 v1, v1, v72, v73
	v_max3_f32 v1, v1, v74, v75
	v_max3_f32 v1, v1, v76, v77
	v_mfma_f32_32x32x16_bf16 v[2:17], v[168:171], v[228:231], v[2:17]
	v_max3_f32 v1, v1, v78, v79
	v_max3_f32 v1, v1, v80, v81
	v_mov_b32_e32 v162, v1
	s_nop 1
	v_permlane32_swap_b32_e32 v1, v162
	v_max_f32_e32 v162, v162, v162
	v_max_f32_e32 v1, v1, v1
	v_max_f32_e32 v1, v1, v162
	v_max_f32_e32 v162, v166, v166
	v_max_f32_e32 v162, v162, v1
	v_sub_f32_e32 v163, v1, v166
	v_mfma_f32_32x32x16_bf16 v[2:17], v[216:219], v[236:239], v[2:17]
	v_sub_f32_e32 v1, v166, v162
	v_mul_f32_e32 v1, 0x3e0293ee, v1
	v_exp_f32_e32 v1, v1
	v_cmp_ge_f32_e32 vcc, s22, v163
	s_cmp_eq_u64 vcc, exec
	s_cselect_b64 s[2:3], -1, 0
	s_barrier
	s_waitcnt vmcnt(4)
	v_cndmask_b32_e64 v216, v1, 1.0, s[2:3]
	v_cmp_gt_f32_e32 vcc, 1.0, v216
	s_waitcnt vmcnt(4)
	ds_write_b128 v203, v[130:133]
	ds_write_b128 v204, v[134:137]
	ds_write_b128 v201, v[138:141] offset:32768
	ds_write_b128 v202, v[142:145] offset:32768
	s_cmp_lt_u32 s79, 33
	s_cbranch_scc0 .Lil_end
	s_cmp_eq_u32 s89, 0
	s_cbranch_scc1 .Lil_issue
	v_lshlrev_b32_e32 v242, 4, v254
	v_add_u32_e32 v242, s87, v242
	v_lshlrev_b32_e32 v243, 3, v254
	v_add_u32_e32 v243, s88, v243
	s_bitcmp1_b32 s79, 0
	s_cbranch_scc0 .Lil_c1
	ds_read_b64 v[244:245], v242 offset:0
	ds_read_b64 v[246:247], v242 offset:1024
	ds_read_b64 v[248:249], v242 offset:2048
	ds_read_b64 v[250:251], v242 offset:3072
	s_waitcnt lgkmcnt(3)
	v_mul_f32_e32 v244, 0x41800000, v244
	v_mul_f32_e32 v245, 0x41800000, v245
	v_max_f32_e32 v244, 0xc3e00000, v244
	v_max_f32_e32 v245, 0xc3e00000, v245
	v_min_f32_e32 v244, 0x43e00000, v244
	v_min_f32_e32 v245, 0x43e00000, v245
	s_waitcnt lgkmcnt(2)
	v_mul_f32_e32 v246, 0x41800000, v246
	v_mul_f32_e32 v247, 0x41800000, v247
	v_max_f32_e32 v246, 0xc3e00000, v246
	v_max_f32_e32 v247, 0xc3e00000, v247
	v_min_f32_e32 v246, 0x43e00000, v246
	v_min_f32_e32 v247, 0x43e00000, v247
	s_waitcnt lgkmcnt(1)
	v_mul_f32_e32 v248, 0x41800000, v248
	v_mul_f32_e32 v249, 0x41800000, v249
	v_max_f32_e32 v248, 0xc3e00000, v248
	v_max_f32_e32 v249, 0xc3e00000, v249
	v_min_f32_e32 v248, 0x43e00000, v248
	v_min_f32_e32 v249, 0x43e00000, v249
	s_waitcnt lgkmcnt(0)
	v_mul_f32_e32 v250, 0x41800000, v250
	v_mul_f32_e32 v251, 0x41800000, v251
	v_max_f32_e32 v250, 0xc3e00000, v250
	v_max_f32_e32 v251, 0xc3e00000, v251
	v_min_f32_e32 v250, 0x43e00000, v250
	v_min_f32_e32 v251, 0x43e00000, v251
	v_cvt_pk_fp8_f32 v252, v244, v246
	v_cvt_pk_fp8_f32 v253, v245, v247
	v_cvt_pk_fp8_f32 v252, v248, v250 op_sel:[0,0,1]
	v_cvt_pk_fp8_f32 v253, v249, v251 op_sel:[0,0,1]
	s_nop 0
	ds_write_b32 v243, v252 offset:0
	ds_write_b32 v243, v253 offset:512
	ds_read_b64 v[244:245], v242 offset:4096
	ds_read_b64 v[246:247], v242 offset:5120
	ds_read_b64 v[248:249], v242 offset:6144
	ds_read_b64 v[250:251], v242 offset:7168
	s_waitcnt lgkmcnt(3)
	v_mul_f32_e32 v244, 0x41800000, v244
	v_mul_f32_e32 v245, 0x41800000, v245
	v_max_f32_e32 v244, 0xc3e00000, v244
	v_max_f32_e32 v245, 0xc3e00000, v245
	v_min_f32_e32 v244, 0x43e00000, v244
	v_min_f32_e32 v245, 0x43e00000, v245
	s_waitcnt lgkmcnt(2)
	v_mul_f32_e32 v246, 0x41800000, v246
	v_mul_f32_e32 v247, 0x41800000, v247
	v_max_f32_e32 v246, 0xc3e00000, v246
	v_max_f32_e32 v247, 0xc3e00000, v247
	v_min_f32_e32 v246, 0x43e00000, v246
	v_min_f32_e32 v247, 0x43e00000, v247
	s_waitcnt lgkmcnt(1)
	v_mul_f32_e32 v248, 0x41800000, v248
	v_mul_f32_e32 v249, 0x41800000, v249
	v_max_f32_e32 v248, 0xc3e00000, v248
	v_max_f32_e32 v249, 0xc3e00000, v249
	v_min_f32_e32 v248, 0x43e00000, v248
	v_min_f32_e32 v249, 0x43e00000, v249
	s_waitcnt lgkmcnt(0)
	v_mul_f32_e32 v250, 0x41800000, v250
	v_mul_f32_e32 v251, 0x41800000, v251
	v_max_f32_e32 v250, 0xc3e00000, v250
	v_max_f32_e32 v251, 0xc3e00000, v251
	v_min_f32_e32 v250, 0x43e00000, v250
	v_min_f32_e32 v251, 0x43e00000, v251
	v_cvt_pk_fp8_f32 v252, v244, v246
	v_cvt_pk_fp8_f32 v253, v245, v247
	v_cvt_pk_fp8_f32 v252, v248, v250 op_sel:[0,0,1]
	v_cvt_pk_fp8_f32 v253, v249, v251 op_sel:[0,0,1]
	s_nop 0
	ds_write_b32 v243, v252 offset:4
	ds_write_b32 v243, v253 offset:516
	ds_read_b64 v[244:245], v242 offset:8
	ds_read_b64 v[246:247], v242 offset:1032
	ds_read_b64 v[248:249], v242 offset:2056
	ds_read_b64 v[250:251], v242 offset:3080
	s_waitcnt lgkmcnt(3)
	v_mul_f32_e32 v244, 0x41800000, v244
	v_mul_f32_e32 v245, 0x41800000, v245
	v_max_f32_e32 v244, 0xc3e00000, v244
	v_max_f32_e32 v245, 0xc3e00000, v245
	v_min_f32_e32 v244, 0x43e00000, v244
	v_min_f32_e32 v245, 0x43e00000, v245
	s_waitcnt lgkmcnt(2)
	v_mul_f32_e32 v246, 0x41800000, v246
	v_mul_f32_e32 v247, 0x41800000, v247
	v_max_f32_e32 v246, 0xc3e00000, v246
	v_max_f32_e32 v247, 0xc3e00000, v247
	v_min_f32_e32 v246, 0x43e00000, v246
	v_min_f32_e32 v247, 0x43e00000, v247
	s_waitcnt lgkmcnt(1)
	v_mul_f32_e32 v248, 0x41800000, v248
	v_mul_f32_e32 v249, 0x41800000, v249
	v_max_f32_e32 v248, 0xc3e00000, v248
	v_max_f32_e32 v249, 0xc3e00000, v249
	v_min_f32_e32 v248, 0x43e00000, v248
	v_min_f32_e32 v249, 0x43e00000, v249
	s_waitcnt lgkmcnt(0)
	v_mul_f32_e32 v250, 0x41800000, v250
	v_mul_f32_e32 v251, 0x41800000, v251
	v_max_f32_e32 v250, 0xc3e00000, v250
	v_max_f32_e32 v251, 0xc3e00000, v251
	v_min_f32_e32 v250, 0x43e00000, v250
	v_min_f32_e32 v251, 0x43e00000, v251
	v_cvt_pk_fp8_f32 v252, v244, v246
	v_cvt_pk_fp8_f32 v253, v245, v247
	v_cvt_pk_fp8_f32 v252, v248, v250 op_sel:[0,0,1]
	v_cvt_pk_fp8_f32 v253, v249, v251 op_sel:[0,0,1]
	s_nop 0
	ds_write_b32 v243, v252 offset:1024
	ds_write_b32 v243, v253 offset:1536
	ds_read_b64 v[244:245], v242 offset:4104
	ds_read_b64 v[246:247], v242 offset:5128
	ds_read_b64 v[248:249], v242 offset:6152
	ds_read_b64 v[250:251], v242 offset:7176
	s_waitcnt lgkmcnt(3)
	v_mul_f32_e32 v244, 0x41800000, v244
	v_mul_f32_e32 v245, 0x41800000, v245
	v_max_f32_e32 v244, 0xc3e00000, v244
	v_max_f32_e32 v245, 0xc3e00000, v245
	v_min_f32_e32 v244, 0x43e00000, v244
	v_min_f32_e32 v245, 0x43e00000, v245
	s_waitcnt lgkmcnt(2)
	v_mul_f32_e32 v246, 0x41800000, v246
	v_mul_f32_e32 v247, 0x41800000, v247
	v_max_f32_e32 v246, 0xc3e00000, v246
	v_max_f32_e32 v247, 0xc3e00000, v247
	v_min_f32_e32 v246, 0x43e00000, v246
	v_min_f32_e32 v247, 0x43e00000, v247
	s_waitcnt lgkmcnt(1)
	v_mul_f32_e32 v248, 0x41800000, v248
	v_mul_f32_e32 v249, 0x41800000, v249
	v_max_f32_e32 v248, 0xc3e00000, v248
	v_max_f32_e32 v249, 0xc3e00000, v249
	v_min_f32_e32 v248, 0x43e00000, v248
	v_min_f32_e32 v249, 0x43e00000, v249
	s_waitcnt lgkmcnt(0)
	v_mul_f32_e32 v250, 0x41800000, v250
	v_mul_f32_e32 v251, 0x41800000, v251
	v_max_f32_e32 v250, 0xc3e00000, v250
	v_max_f32_e32 v251, 0xc3e00000, v251
	v_min_f32_e32 v250, 0x43e00000, v250
	v_min_f32_e32 v251, 0x43e00000, v251
	v_cvt_pk_fp8_f32 v252, v244, v246
	v_cvt_pk_fp8_f32 v253, v245, v247
	v_cvt_pk_fp8_f32 v252, v248, v250 op_sel:[0,0,1]
	v_cvt_pk_fp8_f32 v253, v249, v251 op_sel:[0,0,1]
	s_nop 0
	ds_write_b32 v243, v252 offset:1028
	ds_write_b32 v243, v253 offset:1540
	s_branch .Lil_issue
.Lil_c1:
	s_mov_b32 s90, s84
	s_mov_b32 s91, s85
	ds_read_b64 v[244:245], v242 offset:0
	ds_read_b64 v[246:247], v242 offset:1024
	ds_read_b64 v[248:249], v242 offset:2048
	ds_read_b64 v[250:251], v242 offset:3072
	s_waitcnt lgkmcnt(3)
	v_mul_f32_e32 v244, 0x41800000, v244
	v_mul_f32_e32 v245, 0x41800000, v245
	v_max_f32_e32 v244, 0xc3e00000, v244
	v_max_f32_e32 v245, 0xc3e00000, v245
	v_min_f32_e32 v244, 0x43e00000, v244
	v_min_f32_e32 v245, 0x43e00000, v245
	s_waitcnt lgkmcnt(2)
	v_mul_f32_e32 v246, 0x41800000, v246
	v_mul_f32_e32 v247, 0x41800000, v247
	v_max_f32_e32 v246, 0xc3e00000, v246
	v_max_f32_e32 v247, 0xc3e00000, v247
	v_min_f32_e32 v246, 0x43e00000, v246
	v_min_f32_e32 v247, 0x43e00000, v247
	s_waitcnt lgkmcnt(1)
	v_mul_f32_e32 v248, 0x41800000, v248
	v_mul_f32_e32 v249, 0x41800000, v249
	v_max_f32_e32 v248, 0xc3e00000, v248
	v_max_f32_e32 v249, 0xc3e00000, v249
	v_min_f32_e32 v248, 0x43e00000, v248
	v_min_f32_e32 v249, 0x43e00000, v249
	s_waitcnt lgkmcnt(0)
	v_mul_f32_e32 v250, 0x41800000, v250
	v_mul_f32_e32 v251, 0x41800000, v251
	v_max_f32_e32 v250, 0xc3e00000, v250
	v_max_f32_e32 v251, 0xc3e00000, v251
	v_min_f32_e32 v250, 0x43e00000, v250
	v_min_f32_e32 v251, 0x43e00000, v251
	v_cvt_pk_fp8_f32 v252, v244, v246
	v_cvt_pk_fp8_f32 v253, v245, v247
	v_cvt_pk_fp8_f32 v252, v248, v250 op_sel:[0,0,1]
	v_cvt_pk_fp8_f32 v253, v249, v251 op_sel:[0,0,1]
	ds_read_b64 v[244:245], v242 offset:4096
	ds_read_b64 v[246:247], v242 offset:5120
	ds_read_b64 v[248:249], v242 offset:6144
	ds_read_b64 v[250:251], v242 offset:7168
	s_waitcnt lgkmcnt(3)
	v_mul_f32_e32 v244, 0x41800000, v244
	v_mul_f32_e32 v245, 0x41800000, v245
	v_max_f32_e32 v244, 0xc3e00000, v244
	v_max_f32_e32 v245, 0xc3e00000, v245
	v_min_f32_e32 v244, 0x43e00000, v244
	v_min_f32_e32 v245, 0x43e00000, v245
	s_waitcnt lgkmcnt(2)
	v_mul_f32_e32 v246, 0x41800000, v246
	v_mul_f32_e32 v247, 0x41800000, v247
	v_max_f32_e32 v246, 0xc3e00000, v246
	v_max_f32_e32 v247, 0xc3e00000, v247
	v_min_f32_e32 v246, 0x43e00000, v246
	v_min_f32_e32 v247, 0x43e00000, v247
	s_waitcnt lgkmcnt(1)
	v_mul_f32_e32 v248, 0x41800000, v248
	v_mul_f32_e32 v249, 0x41800000, v249
	v_max_f32_e32 v248, 0xc3e00000, v248
	v_max_f32_e32 v249, 0xc3e00000, v249
	v_min_f32_e32 v248, 0x43e00000, v248
	v_min_f32_e32 v249, 0x43e00000, v249
	s_waitcnt lgkmcnt(0)
	v_mul_f32_e32 v250, 0x41800000, v250
	v_mul_f32_e32 v251, 0x41800000, v251
	v_max_f32_e32 v250, 0xc3e00000, v250
	v_max_f32_e32 v251, 0xc3e00000, v251
	v_min_f32_e32 v250, 0x43e00000, v250
	v_min_f32_e32 v251, 0x43e00000, v251
	v_cvt_pk_fp8_f32 v244, v244, v246
	v_cvt_pk_fp8_f32 v245, v245, v247
	v_cvt_pk_fp8_f32 v244, v248, v250 op_sel:[0,0,1]
	v_cvt_pk_fp8_f32 v245, v249, v251 op_sel:[0,0,1]
	v_and_b32_e32 v247, 7, v254
	v_lshlrev_b32_e32 v247, 2, v247
	v_lshrrev_b32_e32 v246, 3, v254
	v_lshlrev_b32_e32 v246, 4, v246
	v_mad_u32_u24 v246, v247, s86, v246
	ds_read_b64 v[248:249], v243 offset:0
	v_mov_b32_e32 v250, v252
	v_mov_b32_e32 v251, v244
	s_waitcnt lgkmcnt(0)
	global_store_dwordx4 v246, v[248:251], s[90:91] nt
	s_add_u32 s90, s90, s86
	s_addc_u32 s91, s91, 0
	s_nop 1
	ds_read_b64 v[248:249], v243 offset:512
	v_mov_b32_e32 v250, v253
	v_mov_b32_e32 v251, v245
	s_waitcnt lgkmcnt(0)
	global_store_dwordx4 v246, v[248:251], s[90:91] nt
	s_add_u32 s90, s90, s86
	s_addc_u32 s91, s91, 0
	s_nop 1
	ds_read_b64 v[244:245], v242 offset:8
	ds_read_b64 v[246:247], v242 offset:1032
	ds_read_b64 v[248:249], v242 offset:2056
	ds_read_b64 v[250:251], v242 offset:3080
	s_waitcnt lgkmcnt(3)
	v_mul_f32_e32 v244, 0x41800000, v244
	v_mul_f32_e32 v245, 0x41800000, v245
	v_max_f32_e32 v244, 0xc3e00000, v244
	v_max_f32_e32 v245, 0xc3e00000, v245
	v_min_f32_e32 v244, 0x43e00000, v244
	v_min_f32_e32 v245, 0x43e00000, v245
	s_waitcnt lgkmcnt(2)
	v_mul_f32_e32 v246, 0x41800000, v246
	v_mul_f32_e32 v247, 0x41800000, v247
	v_max_f32_e32 v246, 0xc3e00000, v246
	v_max_f32_e32 v247, 0xc3e00000, v247
	v_min_f32_e32 v246, 0x43e00000, v246
	v_min_f32_e32 v247, 0x43e00000, v247
	s_waitcnt lgkmcnt(1)
	v_mul_f32_e32 v248, 0x41800000, v248
	v_mul_f32_e32 v249, 0x41800000, v249
	v_max_f32_e32 v248, 0xc3e00000, v248
	v_max_f32_e32 v249, 0xc3e00000, v249
	v_min_f32_e32 v248, 0x43e00000, v248
	v_min_f32_e32 v249, 0x43e00000, v249
	s_waitcnt lgkmcnt(0)
	v_mul_f32_e32 v250, 0x41800000, v250
	v_mul_f32_e32 v251, 0x41800000, v251
	v_max_f32_e32 v250, 0xc3e00000, v250
	v_max_f32_e32 v251, 0xc3e00000, v251
	v_min_f32_e32 v250, 0x43e00000, v250
	v_min_f32_e32 v251, 0x43e00000, v251
	v_cvt_pk_fp8_f32 v252, v244, v246
	v_cvt_pk_fp8_f32 v253, v245, v247
	v_cvt_pk_fp8_f32 v252, v248, v250 op_sel:[0,0,1]
	v_cvt_pk_fp8_f32 v253, v249, v251 op_sel:[0,0,1]
	ds_read_b64 v[244:245], v242 offset:4104
	ds_read_b64 v[246:247], v242 offset:5128
	ds_read_b64 v[248:249], v242 offset:6152
	ds_read_b64 v[250:251], v242 offset:7176
	s_waitcnt lgkmcnt(3)
	v_mul_f32_e32 v244, 0x41800000, v244
	v_mul_f32_e32 v245, 0x41800000, v245
	v_max_f32_e32 v244, 0xc3e00000, v244
	v_max_f32_e32 v245, 0xc3e00000, v245
	v_min_f32_e32 v244, 0x43e00000, v244
	v_min_f32_e32 v245, 0x43e00000, v245
	s_waitcnt lgkmcnt(2)
	v_mul_f32_e32 v246, 0x41800000, v246
	v_mul_f32_e32 v247, 0x41800000, v247
	v_max_f32_e32 v246, 0xc3e00000, v246
	v_max_f32_e32 v247, 0xc3e00000, v247
	v_min_f32_e32 v246, 0x43e00000, v246
	v_min_f32_e32 v247, 0x43e00000, v247
	s_waitcnt lgkmcnt(1)
	v_mul_f32_e32 v248, 0x41800000, v248
	v_mul_f32_e32 v249, 0x41800000, v249
	v_max_f32_e32 v248, 0xc3e00000, v248
	v_max_f32_e32 v249, 0xc3e00000, v249
	v_min_f32_e32 v248, 0x43e00000, v248
	v_min_f32_e32 v249, 0x43e00000, v249
	s_waitcnt lgkmcnt(0)
	v_mul_f32_e32 v250, 0x41800000, v250
	v_mul_f32_e32 v251, 0x41800000, v251
	v_max_f32_e32 v250, 0xc3e00000, v250
	v_max_f32_e32 v251, 0xc3e00000, v251
	v_min_f32_e32 v250, 0x43e00000, v250
	v_min_f32_e32 v251, 0x43e00000, v251
	v_cvt_pk_fp8_f32 v244, v244, v246
	v_cvt_pk_fp8_f32 v245, v245, v247
	v_cvt_pk_fp8_f32 v244, v248, v250 op_sel:[0,0,1]
	v_cvt_pk_fp8_f32 v245, v249, v251 op_sel:[0,0,1]
	v_and_b32_e32 v247, 7, v254
	v_lshlrev_b32_e32 v247, 2, v247
	v_lshrrev_b32_e32 v246, 3, v254
	v_lshlrev_b32_e32 v246, 4, v246
	v_mad_u32_u24 v246, v247, s86, v246
	ds_read_b64 v[248:249], v243 offset:1024
	v_mov_b32_e32 v250, v252
	v_mov_b32_e32 v251, v244
	s_waitcnt lgkmcnt(0)
	global_store_dwordx4 v246, v[248:251], s[90:91] nt
	s_add_u32 s90, s90, s86
	s_addc_u32 s91, s91, 0
	s_nop 1
	ds_read_b64 v[248:249], v243 offset:1536
	v_mov_b32_e32 v250, v253
	v_mov_b32_e32 v251, v245
	s_waitcnt lgkmcnt(0)
	global_store_dwordx4 v246, v[248:251], s[90:91] nt
	s_add_u32 s90, s90, s86
	s_addc_u32 s91, s91, 0
	s_nop 1
.Lil_issue:
	s_mov_b32 s89, 0
	s_cmp_lt_u32 s79, 32
	s_cbranch_scc0 .Lil_inc
	s_cmp_lt_u32 s77, s78
	s_cbranch_scc0 .Lil_inc
	s_bitcmp1_b32 s79, 0
	s_cbranch_scc1 .Lil_h1
	s_cmp_lt_u32 s77, 0x8000
	s_cbranch_scc0 .Lil_dn_a
	s_lshr_b32 s90, s77, 14
	s_and_b32 s91, s77, 0x3fff
	s_cmp_eq_u32 s90, 0
	s_cselect_b32 s80, s36, s38
	s_cselect_b32 s81, s37, s39
	s_lshr_b32 s92, s91, 8
	s_and_b32 s93, s91, 0xff
	s_lshr_b32 s91, s93, 4
	s_and_b32 s93, s93, 15
	s_lshl_b32 s94, s92, 22
	s_lshl_b32 s83, s91, 18
	s_add_u32 s94, s94, s83
	s_lshl_b32 s83, s93, 7
	s_add_u32 s94, s94, s83
	s_add_u32 s80, s80, s94
	s_addc_u32 s81, s81, 0
	s_movk_i32 s82, 0x800
	s_lshl_b32 s94, s92, 10
	s_lshr_b32 s83, s93, 2
	s_lshl_b32 s83, s83, 8
	s_add_u32 s94, s94, s83
	s_lshl_b32 s83, s90, 7
	s_add_u32 s94, s94, s83
	s_and_b32 s83, s93, 3
	s_lshl_b32 s83, s83, 5
	s_add_u32 s94, s94, s83
	s_lshl_b32 s94, s94, 11
	s_lshl_b32 s83, s91, 7
	s_add_u32 s94, s94, s83
	s_add_u32 s84, s50, 0x1c200000
	s_addc_u32 s85, s51, 0
	s_add_u32 s84, s84, s94
	s_addc_u32 s85, s85, 0
	s_movk_i32 s86, 0x800
	s_branch .Lil_ad_a
.Lil_dn_a:
	s_sub_u32 s91, s77, 0x8000
	s_lshr_b32 s92, s91, 8
	s_and_b32 s93, s91, 0xff
	s_lshr_b32 s91, s93, 6
	s_and_b32 s93, s93, 63
	s_lshl_b32 s94, s92, 22
	s_lshl_b32 s83, s91, 20
	s_add_u32 s94, s94, s83
	s_lshl_b32 s83, s93, 7
	s_add_u32 s94, s94, s83
	s_add_u32 s80, s40, s94
	s_addc_u32 s81, s41, 0
	s_movk_i32 s82, 0x2000
	s_lshl_b32 s94, s92, 11
	s_lshl_b32 s83, s93, 5
	s_add_u32 s94, s94, s83
	s_lshl_b32 s94, s94, 9
	s_lshl_b32 s83, s91, 7
	s_add_u32 s94, s94, s83
	s_add_u32 s84, s50, 0x2c600000
	s_addc_u32 s85, s51, 0
	s_add_u32 s84, s84, s94
	s_addc_u32 s85, s85, 0
	s_movk_i32 s86, 0x200
.Lil_ad_a:
	s_mov_b32 s92, s80
	s_mov_b32 s93, s81
	s_branch .Lil_ld
.Lil_h1:
	s_lshl_b32 s90, s82, 3
	s_add_u32 s92, s80, s90
	s_addc_u32 s93, s81, 0
	s_add_u32 s77, s77, 8
.Lil_ld:
	v_lshrrev_b32_e32 v244, 3, v254
	v_lshlrev_b32_e32 v244, 4, v244
	v_and_b32_e32 v245, 7, v254
	v_lshlrev_b32_e32 v245, 4, v245
	v_mad_u32_u24 v244, v244, s82, v245
	s_mov_b32 s94, s87
	s_mov_b32 s89, 1
.Lil_inc:
	s_add_u32 s79, s79, 1
.Lil_end:
	s_cbranch_vccz .LBB0_1145
	s_and_saveexec_b64 s[18:19], s[0:1]
	ds_write_b32 v197, v216 offset:128
	s_or_b64 exec, exec, s[18:19]
	s_waitcnt lgkmcnt(0)
	v_add_u32_e32 v1, v196, v182
	ds_read_b128 v[168:171], v1 offset:224
	ds_read_b128 v[172:175], v1 offset:192
	ds_read_b128 v[218:221], v1 offset:160
	ds_read_b128 v[222:225], v1 offset:128
	s_waitcnt lgkmcnt(3)
	v_pk_mul_f32 v[30:31], v[30:31], v[168:169]
	s_waitcnt lgkmcnt(2)
	v_pk_mul_f32 v[26:27], v[26:27], v[172:173]
	s_waitcnt lgkmcnt(1)
	v_pk_mul_f32 v[22:23], v[22:23], v[218:219]
	v_pk_mul_f32 v[32:33], v[32:33], v[170:171]
	v_pk_mul_f32 v[28:29], v[28:29], v[174:175]
	v_pk_mul_f32 v[24:25], v[24:25], v[220:221]
	s_waitcnt lgkmcnt(0)
	v_pk_mul_f32 v[20:21], v[20:21], v[224:225]
	v_pk_mul_f32 v[18:19], v[18:19], v[222:223]
	v_pk_mul_f32 v[62:63], v[62:63], v[168:169]
	v_pk_mul_f32 v[58:59], v[58:59], v[172:173]
	v_pk_mul_f32 v[54:55], v[54:55], v[218:219]
	v_pk_mul_f32 v[64:65], v[64:65], v[170:171]
	v_pk_mul_f32 v[60:61], v[60:61], v[174:175]
	v_pk_mul_f32 v[56:57], v[56:57], v[220:221]
	v_pk_mul_f32 v[52:53], v[52:53], v[224:225]
	v_pk_mul_f32 v[50:51], v[50:51], v[222:223]
	v_pk_mul_f32 v[46:47], v[46:47], v[168:169]
	v_pk_mul_f32 v[42:43], v[42:43], v[172:173]
	v_pk_mul_f32 v[38:39], v[38:39], v[218:219]
	v_pk_mul_f32 v[48:49], v[48:49], v[170:171]
	v_pk_mul_f32 v[44:45], v[44:45], v[174:175]
	v_pk_mul_f32 v[40:41], v[40:41], v[220:221]
	v_pk_mul_f32 v[36:37], v[36:37], v[224:225]
	v_pk_mul_f32 v[34:35], v[34:35], v[222:223]
	v_pk_mul_f32 v[14:15], v[14:15], v[168:169]
	v_pk_mul_f32 v[10:11], v[10:11], v[172:173]
	v_pk_mul_f32 v[6:7], v[6:7], v[218:219]
	v_pk_mul_f32 v[16:17], v[16:17], v[170:171]
	v_pk_mul_f32 v[12:13], v[12:13], v[174:175]
	v_pk_mul_f32 v[8:9], v[8:9], v[220:221]
	v_pk_mul_f32 v[4:5], v[4:5], v[224:225]
	v_pk_mul_f32 v[2:3], v[2:3], v[222:223]
.LBB0_1145:
	v_cndmask_b32_e64 v217, v162, v166, s[2:3]
	v_mul_f32_e32 v218, 0xbe0293ee, v217
	v_fmamk_f32 v1, v82, 0x3e0293ee, v218
	v_fmamk_f32 v82, v83, 0x3e0293ee, v218
	v_fmamk_f32 v83, v84, 0x3e0293ee, v218
	v_fmamk_f32 v84, v85, 0x3e0293ee, v218
	v_fmamk_f32 v85, v86, 0x3e0293ee, v218
	v_fmamk_f32 v86, v87, 0x3e0293ee, v218
	v_fmamk_f32 v87, v88, 0x3e0293ee, v218
	v_fmamk_f32 v88, v89, 0x3e0293ee, v218
	v_fmamk_f32 v89, v90, 0x3e0293ee, v218
	v_fmamk_f32 v90, v91, 0x3e0293ee, v218
	v_fmamk_f32 v91, v92, 0x3e0293ee, v218
	v_fmamk_f32 v92, v93, 0x3e0293ee, v218
	v_fmamk_f32 v93, v94, 0x3e0293ee, v218
	v_fmamk_f32 v94, v95, 0x3e0293ee, v218
	v_fmamk_f32 v95, v96, 0x3e0293ee, v218
	v_fmamk_f32 v96, v97, 0x3e0293ee, v218
	v_exp_f32_e32 v162, v1
	v_exp_f32_e32 v177, v82
	v_exp_f32_e32 v163, v83
	v_exp_f32_e32 v176, v84
	v_exp_f32_e32 v164, v85
	v_exp_f32_e32 v175, v86
	v_exp_f32_e32 v165, v87
	v_exp_f32_e32 v174, v88
	v_exp_f32_e32 v166, v89
	v_exp_f32_e32 v173, v90
	v_exp_f32_e32 v167, v91
	v_exp_f32_e32 v172, v92
	v_exp_f32_e32 v168, v93
	v_exp_f32_e32 v171, v94
	v_exp_f32_e32 v169, v95
	v_exp_f32_e32 v170, v96
	v_fmamk_f32 v227, v66, 0x3e0293ee, v218
	v_fmamk_f32 v228, v67, 0x3e0293ee, v218
	v_fmamk_f32 v229, v68, 0x3e0293ee, v218
	v_fmamk_f32 v230, v69, 0x3e0293ee, v218
	v_fmamk_f32 v231, v70, 0x3e0293ee, v218
	v_fmamk_f32 v220, v71, 0x3e0293ee, v218
	v_fmamk_f32 v221, v72, 0x3e0293ee, v218
	v_fmamk_f32 v222, v73, 0x3e0293ee, v218
	v_fmamk_f32 v223, v74, 0x3e0293ee, v218
	v_fmamk_f32 v224, v75, 0x3e0293ee, v218
	v_fmamk_f32 v225, v76, 0x3e0293ee, v218
	v_fmamk_f32 v226, v77, 0x3e0293ee, v218
	v_fmamk_f32 v219, v78, 0x3e0293ee, v218
	v_fmamk_f32 v232, v79, 0x3e0293ee, v218
	v_fmamk_f32 v233, v80, 0x3e0293ee, v218
	v_fmac_f32_e32 v218, 0x3e0293ee, v81
	s_waitcnt lgkmcnt(0)
	s_barrier
	s_cmp_eq_u32 s89, 0
	s_cbranch_scc1 .Lil_b2end
	s_mov_b32 m0, s94
	s_add_u32 s94, s94, 0x400
	global_load_lds_dwordx4 v244, s[92:93] nt
	s_add_u32 s92, s92, s82
	s_addc_u32 s93, s93, 0
	s_mov_b32 m0, s94
	s_add_u32 s94, s94, 0x400
	global_load_lds_dwordx4 v244, s[92:93] nt
	s_add_u32 s92, s92, s82
	s_addc_u32 s93, s93, 0
	s_mov_b32 m0, s94
	s_add_u32 s94, s94, 0x400
	global_load_lds_dwordx4 v244, s[92:93] nt
	s_add_u32 s92, s92, s82
	s_addc_u32 s93, s93, 0
	s_mov_b32 m0, s94
	s_add_u32 s94, s94, 0x400
	global_load_lds_dwordx4 v244, s[92:93] nt
	s_add_u32 s92, s92, s82
	s_addc_u32 s93, s93, 0
	s_mov_b32 m0, s94
	s_add_u32 s94, s94, 0x400
	global_load_lds_dwordx4 v244, s[92:93] nt
	s_add_u32 s92, s92, s82
	s_addc_u32 s93, s93, 0
	s_mov_b32 m0, s94
	s_add_u32 s94, s94, 0x400
	global_load_lds_dwordx4 v244, s[92:93] nt
	s_add_u32 s92, s92, s82
	s_addc_u32 s93, s93, 0
	s_mov_b32 m0, s94
	s_add_u32 s94, s94, 0x400
	global_load_lds_dwordx4 v244, s[92:93] nt
	s_add_u32 s92, s92, s82
	s_addc_u32 s93, s93, 0
	s_mov_b32 m0, s94
	s_add_u32 s94, s94, 0x400
	global_load_lds_dwordx4 v244, s[92:93] nt
.Lil_b2end:
	ds_read_b128 v[66:69], v205 offset:32768
	ds_read_b128 v[70:73], v205 offset:40960
	ds_read_b128 v[234:237], v206 offset:32768
	ds_read_b128 v[238:241], v206 offset:40960
	v_exp_f32_e32 v1, v227
	v_exp_f32_e32 v227, v229
	s_waitcnt lgkmcnt(3)
	v_mfma_f32_32x32x16_bf16 v[82:97], v[66:69], v[126:129], 0
	v_exp_f32_e32 v229, v231
	v_exp_f32_e32 v231, v232
	v_exp_f32_e32 v232, v233
	v_exp_f32_e32 v233, v218
	v_add_f32_e32 v218, 0, v162
	v_add_f32_e32 v218, v177, v218
	v_add_f32_e32 v218, v163, v218
	s_waitcnt lgkmcnt(2)
	v_mfma_f32_32x32x16_bf16 v[66:81], v[70:73], v[126:129], 0
	v_add_f32_e32 v218, v176, v218
	v_add_f32_e32 v218, v164, v218
	v_add_f32_e32 v218, v175, v218
	v_add_f32_e32 v218, v165, v218
	v_add_f32_e32 v218, v174, v218
	v_add_f32_e32 v218, v166, v218
	v_add_f32_e32 v218, v173, v218
	s_waitcnt lgkmcnt(1)
	v_mfma_f32_32x32x16_bf16 v[82:97], v[234:237], v[114:117], v[82:97]
	v_add_f32_e32 v218, v167, v218
	v_add_f32_e32 v218, v172, v218
	v_add_f32_e32 v218, v168, v218
	v_exp_f32_e32 v200, v228
	v_add_f32_e32 v218, v171, v218
	v_add_f32_e32 v218, v169, v218
	v_exp_f32_e32 v228, v230
	s_waitcnt lgkmcnt(0)
	v_mfma_f32_32x32x16_bf16 v[66:81], v[238:241], v[114:117], v[66:81]
	ds_read_b128 v[234:237], v207 offset:32768
	ds_read_b128 v[238:241], v207 offset:40960
	v_add_f32_e32 v218, v170, v218
	v_add_f32_e32 v218, v1, v218
	v_exp_f32_e32 v220, v220
	v_add_f32_e32 v218, v200, v218
	v_exp_f32_e32 v221, v221
	v_add_f32_e32 v218, v227, v218
	s_waitcnt lgkmcnt(1)
	v_mfma_f32_32x32x16_bf16 v[82:97], v[234:237], v[118:121], v[82:97]
	v_exp_f32_e32 v222, v222
	v_add_f32_e32 v218, v228, v218
	v_exp_f32_e32 v223, v223
	v_add_f32_e32 v218, v229, v218
	v_exp_f32_e32 v224, v224
	v_add_f32_e32 v218, v220, v218
	v_exp_f32_e32 v225, v225
	s_waitcnt lgkmcnt(0)
	v_mfma_f32_32x32x16_bf16 v[66:81], v[238:241], v[118:121], v[66:81]
	ds_read_b128 v[234:237], v208 offset:32768
	ds_read_b128 v[238:241], v208 offset:40960
	v_add_f32_e32 v218, v221, v218
	v_exp_f32_e32 v226, v226
	v_add_f32_e32 v218, v222, v218
	v_exp_f32_e32 v230, v219
	v_add_f32_e32 v218, v223, v218
	v_add_f32_e32 v218, v224, v218
	s_waitcnt lgkmcnt(1)
	v_mfma_f32_32x32x16_bf16 v[82:97], v[234:237], v[122:125], v[82:97]
	v_add_f32_e32 v218, v225, v218
	v_add_f32_e32 v218, v226, v218
	v_add_f32_e32 v218, v230, v218
	v_add_f32_e32 v218, v231, v218
	v_add_f32_e32 v218, v232, v218
	v_add_f32_e32 v218, v233, v218
	v_mov_b32_e32 v219, v218
	s_waitcnt lgkmcnt(0)
	v_mfma_f32_32x32x16_bf16 v[66:81], v[238:241], v[122:125], v[66:81]
	ds_read_b128 v[234:237], v209 offset:32768
	ds_read_b128 v[238:241], v209 offset:40960
	v_permlane32_swap_b32_e32 v218, v219
	s_waitcnt lgkmcnt(1)
	v_mfma_f32_32x32x16_bf16 v[82:97], v[234:237], v[110:113], v[82:97]
	s_waitcnt lgkmcnt(0)
	v_mfma_f32_32x32x16_bf16 v[66:81], v[238:241], v[110:113], v[66:81]
	ds_read_b128 v[234:237], v210 offset:32768
	ds_read_b128 v[238:241], v210 offset:40960
	s_waitcnt lgkmcnt(1)
	v_mfma_f32_32x32x16_bf16 v[82:97], v[234:237], v[106:109], v[82:97]
	s_waitcnt lgkmcnt(0)
	v_mfma_f32_32x32x16_bf16 v[66:81], v[238:241], v[106:109], v[66:81]
	ds_read_b128 v[234:237], v211 offset:32768
	ds_read_b128 v[238:241], v211 offset:40960
	s_waitcnt lgkmcnt(1)
	v_mfma_f32_32x32x16_bf16 v[82:97], v[234:237], v[102:105], v[82:97]
	s_waitcnt lgkmcnt(0)
	v_mfma_f32_32x32x16_bf16 v[66:81], v[238:241], v[102:105], v[66:81]
	ds_read_b128 v[234:237], v212 offset:32768
	ds_read_b128 v[238:241], v212 offset:40960
	v_cvt_pk_bf16_f32 v162, v162, v177
	v_cvt_pk_bf16_f32 v163, v163, v176
	v_cvt_pk_bf16_f32 v164, v164, v175
	v_cvt_pk_bf16_f32 v165, v165, v174
	v_cvt_pk_bf16_f32 v166, v166, v173
	v_cvt_pk_bf16_f32 v167, v167, v172
	s_waitcnt lgkmcnt(1)
	v_mfma_f32_32x32x16_bf16 v[82:97], v[234:237], v[98:101], v[82:97]
	v_cvt_pk_bf16_f32 v168, v168, v171
	v_cvt_pk_bf16_f32 v169, v169, v170
	v_cvt_pk_bf16_f32 v170, v1, v200
	v_cvt_pk_bf16_f32 v171, v227, v228
	v_cvt_pk_bf16_f32 v172, v229, v220
	v_cvt_pk_bf16_f32 v173, v221, v222
	v_cvt_pk_bf16_f32 v174, v223, v224
	s_waitcnt lgkmcnt(0)
	v_mfma_f32_32x32x16_bf16 v[66:81], v[238:241], v[98:101], v[66:81]
	v_cvt_pk_bf16_f32 v175, v225, v226
	v_cvt_pk_bf16_f32 v176, v230, v231
	v_cvt_pk_bf16_f32 v177, v232, v233
	v_permlane32_swap_b32_e32 v162, v164
	v_permlane32_swap_b32_e32 v163, v165
	v_permlane32_swap_b32_e32 v166, v168
	v_permlane32_swap_b32_e32 v167, v169
	v_permlane32_swap_b32_e32 v170, v172
	v_permlane32_swap_b32_e32 v171, v173
	v_permlane32_swap_b32_e32 v174, v176
	v_permlane32_swap_b32_e32 v175, v177
	s_cmp_gt_u32 s15, 64
	s_cselect_b64 s[18:19], -1, 0
	s_and_b64 vcc, exec, s[18:19]
	s_cbranch_vccnz .Lattn_drain0
	v_lshl_add_u64 v[138:139], s[16:17], 0, v[186:187]
	v_add_co_u32_e32 v130, vcc, 0x5f00000, v138
	v_lshl_add_u64 v[140:141], s[16:17], 0, v[184:185]
	s_nop 0
	v_addc_co_u32_e32 v131, vcc, 0, v139, vcc
	v_add_co_u32_e32 v134, vcc, 0x5f00000, v140
	s_nop 1
	v_addc_co_u32_e32 v135, vcc, 0, v141, vcc
	v_add_co_u32_e32 v138, vcc, 0x5600000, v138
	global_load_dwordx4 v[130:133], v[130:131], off
	s_nop 0
	global_load_dwordx4 v[134:137], v[134:135], off
	v_addc_co_u32_e32 v139, vcc, 0, v139, vcc
	v_add_co_u32_e32 v142, vcc, 0x5600000, v140
	s_nop 1
	v_addc_co_u32_e32 v143, vcc, 0, v141, vcc
	global_load_dwordx4 v[138:141], v[138:139], off
	s_nop 0
	global_load_dwordx4 v[142:145], v[142:143], off
.LBB0_1147:
	ds_read_b64_tr_b16 v[220:221], v198 offset:0
	ds_read_b64_tr_b16 v[222:223], v198 offset:0x800
	ds_read_b64_tr_b16 v[224:225], v198 offset:0x1000
	ds_read_b64_tr_b16 v[226:227], v198 offset:0x1800
	ds_read_b64_tr_b16 v[228:229], v198 offset:0x2000
	ds_read_b64_tr_b16 v[230:231], v198 offset:0x2800
	ds_read_b64_tr_b16 v[232:233], v198 offset:0x3000
	ds_read_b64_tr_b16 v[234:235], v198 offset:0x3800
	s_waitcnt lgkmcnt(0)
	s_nop 0
	v_mfma_f32_32x32x16_bf16 v[18:33], v[162:165], v[220:223], v[18:33]
	ds_read_b64_tr_b16 v[220:221], v198 offset:0x200
	ds_read_b64_tr_b16 v[222:223], v198 offset:0xa00
	v_mfma_f32_32x32x16_bf16 v[18:33], v[166:169], v[224:227], v[18:33]
	ds_read_b64_tr_b16 v[224:225], v198 offset:0x1200
	ds_read_b64_tr_b16 v[226:227], v198 offset:0x1a00
	v_mfma_f32_32x32x16_bf16 v[18:33], v[170:173], v[228:231], v[18:33]
	ds_read_b64_tr_b16 v[228:229], v198 offset:0x2200
	ds_read_b64_tr_b16 v[230:231], v198 offset:0x2a00
	ds_read_b64_tr_b16 v[236:237], v198 offset:0x3200
	ds_read_b64_tr_b16 v[238:239], v198 offset:0x3a00
	s_waitcnt lgkmcnt(0)
	v_mfma_f32_32x32x16_bf16 v[18:33], v[174:177], v[232:235], v[18:33]
	v_mfma_f32_32x32x16_bf16 v[50:65], v[162:165], v[220:223], v[50:65]
	ds_read_b64_tr_b16 v[220:221], v198 offset:0x400
	ds_read_b64_tr_b16 v[222:223], v198 offset:0xc00
	v_mfma_f32_32x32x16_bf16 v[50:65], v[166:169], v[224:227], v[50:65]
	ds_read_b64_tr_b16 v[224:225], v198 offset:0x1400
	ds_read_b64_tr_b16 v[226:227], v198 offset:0x1c00
	v_mfma_f32_32x32x16_bf16 v[50:65], v[170:173], v[228:231], v[50:65]
	ds_read_b64_tr_b16 v[228:229], v198 offset:0x2400
	ds_read_b64_tr_b16 v[230:231], v198 offset:0x2c00
	ds_read_b64_tr_b16 v[232:233], v198 offset:0x3400
	ds_read_b64_tr_b16 v[234:235], v198 offset:0x3c00
	s_waitcnt lgkmcnt(0)
	v_mfma_f32_32x32x16_bf16 v[50:65], v[174:177], v[236:239], v[50:65]
	v_mfma_f32_32x32x16_bf16 v[34:49], v[162:165], v[220:223], v[34:49]
	ds_read_b64_tr_b16 v[220:221], v198 offset:0x600
	ds_read_b64_tr_b16 v[222:223], v198 offset:0xe00
	v_mfma_f32_32x32x16_bf16 v[34:49], v[166:169], v[224:227], v[34:49]
	ds_read_b64_tr_b16 v[224:225], v198 offset:0x1600
	ds_read_b64_tr_b16 v[226:227], v198 offset:0x1e00
	v_mfma_f32_32x32x16_bf16 v[34:49], v[170:173], v[228:231], v[34:49]
	ds_read_b64_tr_b16 v[228:229], v198 offset:0x2600
	ds_read_b64_tr_b16 v[230:231], v198 offset:0x2e00
	ds_read_b64_tr_b16 v[236:237], v198 offset:0x3600
	ds_read_b64_tr_b16 v[238:239], v198 offset:0x3e00
	s_waitcnt lgkmcnt(0)
	v_mfma_f32_32x32x16_bf16 v[34:49], v[174:177], v[232:235], v[34:49]
	v_mfma_f32_32x32x16_bf16 v[2:17], v[162:165], v[220:223], v[2:17]
	v_max_f32_e32 v1, v83, v83
	v_max_f32_e32 v200, v82, v82
	v_max_f32_e32 v1, v200, v1
	v_max3_f32 v1, v1, v84, v85
	v_max3_f32 v1, v1, v86, v87
	v_max3_f32 v1, v1, v88, v89
	v_max3_f32 v1, v1, v90, v91
	v_max3_f32 v1, v1, v92, v93
	v_mfma_f32_32x32x16_bf16 v[2:17], v[166:169], v[224:227], v[2:17]
	v_max3_f32 v1, v1, v94, v95
	v_max3_f32 v1, v1, v96, v97
	v_max3_f32 v1, v1, v66, v67
	v_max3_f32 v1, v1, v68, v69
	v_max3_f32 v1, v1, v70, v71
	v_max3_f32 v1, v1, v72, v73
	v_max3_f32 v1, v1, v74, v75
	v_max3_f32 v1, v1, v76, v77
	v_mfma_f32_32x32x16_bf16 v[2:17], v[170:173], v[228:231], v[2:17]
	v_max3_f32 v1, v1, v78, v79
	v_max3_f32 v1, v1, v80, v81
	v_mov_b32_e32 v162, v1
	s_nop 1
	v_permlane32_swap_b32_e32 v1, v162
	v_max_f32_e32 v162, v162, v162
	v_max_f32_e32 v1, v1, v1
	v_max_f32_e32 v1, v1, v162
	v_max_f32_e32 v163, v217, v217
	v_max_f32_e32 v163, v163, v1
	v_sub_f32_e32 v162, v1, v217
	v_mfma_f32_32x32x16_bf16 v[2:17], v[174:177], v[236:239], v[2:17]
	v_sub_f32_e32 v1, v217, v163
	v_mul_f32_e32 v1, 0x3e0293ee, v1
	v_exp_f32_e32 v1, v1
	v_cmp_ge_f32_e32 vcc, s22, v162
	s_cmp_eq_u64 vcc, exec
	s_cselect_b64 s[2:3], -1, 0
	s_barrier
	s_cmp_eq_u32 s89, 0
	s_cbranch_scc1 .Lil_w2a
	s_waitcnt vmcnt(12)
	s_branch .Lil_w2b
.Lil_w2a:
	s_waitcnt vmcnt(4)
.Lil_w2b:
	v_cndmask_b32_e64 v162, v1, 1.0, s[2:3]
	v_cmp_gt_f32_e32 vcc, 1.0, v162
	ds_write_b128 v203, v[146:149] offset:16384
	ds_write_b128 v204, v[150:153] offset:16384
	ds_write_b128 v201, v[154:157] offset:49152
	ds_write_b128 v202, v[158:161] offset:49152
	s_cbranch_vccz .LBB0_1151
	s_and_saveexec_b64 s[20:21], s[0:1]
	ds_write_b32 v197, v162 offset:128
	s_or_b64 exec, exec, s[20:21]
	s_waitcnt lgkmcnt(0)
	v_add_u32_e32 v1, v196, v182
	ds_read_b128 v[146:149], v1 offset:224
	ds_read_b128 v[150:153], v1 offset:192
	ds_read_b128 v[154:157], v1 offset:160
	ds_read_b128 v[158:161], v1 offset:128
	s_waitcnt lgkmcnt(3)
	v_pk_mul_f32 v[30:31], v[30:31], v[146:147]
	s_waitcnt lgkmcnt(2)
	v_pk_mul_f32 v[26:27], v[26:27], v[150:151]
	s_waitcnt lgkmcnt(1)
	v_pk_mul_f32 v[22:23], v[22:23], v[154:155]
	v_pk_mul_f32 v[32:33], v[32:33], v[148:149]
	v_pk_mul_f32 v[28:29], v[28:29], v[152:153]
	v_pk_mul_f32 v[24:25], v[24:25], v[156:157]
	s_waitcnt lgkmcnt(0)
	v_pk_mul_f32 v[20:21], v[20:21], v[160:161]
	v_pk_mul_f32 v[18:19], v[18:19], v[158:159]
	v_pk_mul_f32 v[62:63], v[62:63], v[146:147]
	v_pk_mul_f32 v[58:59], v[58:59], v[150:151]
	v_pk_mul_f32 v[54:55], v[54:55], v[154:155]
	v_pk_mul_f32 v[64:65], v[64:65], v[148:149]
	v_pk_mul_f32 v[60:61], v[60:61], v[152:153]
	v_pk_mul_f32 v[56:57], v[56:57], v[156:157]
	v_pk_mul_f32 v[52:53], v[52:53], v[160:161]
	v_pk_mul_f32 v[50:51], v[50:51], v[158:159]
	v_pk_mul_f32 v[46:47], v[46:47], v[146:147]
	v_pk_mul_f32 v[42:43], v[42:43], v[150:151]
	v_pk_mul_f32 v[38:39], v[38:39], v[154:155]
	v_pk_mul_f32 v[48:49], v[48:49], v[148:149]
	v_pk_mul_f32 v[44:45], v[44:45], v[152:153]
	v_pk_mul_f32 v[40:41], v[40:41], v[156:157]
	v_pk_mul_f32 v[36:37], v[36:37], v[160:161]
	v_pk_mul_f32 v[34:35], v[34:35], v[158:159]
	v_pk_mul_f32 v[14:15], v[14:15], v[146:147]
	v_pk_mul_f32 v[10:11], v[10:11], v[150:151]
	v_pk_mul_f32 v[6:7], v[6:7], v[154:155]
	v_pk_mul_f32 v[16:17], v[16:17], v[148:149]
	v_pk_mul_f32 v[12:13], v[12:13], v[152:153]
	v_pk_mul_f32 v[8:9], v[8:9], v[156:157]
	v_pk_mul_f32 v[4:5], v[4:5], v[160:161]
	v_pk_mul_f32 v[2:3], v[2:3], v[158:159]

	.amdhsa_kernel _ZN2mk3fwdENS_4ArgsE
		.amdhsa_group_segment_fixed_size 16384
		.amdhsa_private_segment_fixed_size 0
		.amdhsa_kernarg_size 472
		.amdhsa_user_sgpr_count 2
		.amdhsa_user_sgpr_dispatch_ptr 0
		.amdhsa_user_sgpr_queue_ptr 0
		.amdhsa_user_sgpr_kernarg_segment_ptr 1
		.amdhsa_user_sgpr_dispatch_id 0
		.amdhsa_user_sgpr_kernarg_preload_length 0
		.amdhsa_user_sgpr_kernarg_preload_offset 0
		.amdhsa_user_sgpr_private_segment_size 0
		.amdhsa_uses_dynamic_stack 0
		.amdhsa_enable_private_segment 0
		.amdhsa_system_sgpr_workgroup_id_x 1
		.amdhsa_system_sgpr_workgroup_id_y 0
		.amdhsa_system_sgpr_workgroup_id_z 0
		.amdhsa_system_sgpr_workgroup_info 0
		.amdhsa_system_vgpr_workitem_id 0
		.amdhsa_next_free_vgpr 256
		.amdhsa_next_free_sgpr 98
		.amdhsa_accum_offset 256
		.amdhsa_reserve_vcc 1
		.amdhsa_float_round_mode_32 0
		.amdhsa_float_round_mode_16_64 0
		.amdhsa_float_denorm_mode_32 3
		.amdhsa_float_denorm_mode_16_64 3
		.amdhsa_dx10_clamp 1
		.amdhsa_ieee_mode 1
		.amdhsa_fp16_overflow 0
		.amdhsa_tg_split 0
		.amdhsa_exception_fp_ieee_invalid_op 0
		.amdhsa_exception_fp_denorm_src 0
		.amdhsa_exception_fp_ieee_div_zero 0
		.amdhsa_exception_fp_ieee_overflow 0
		.amdhsa_exception_fp_ieee_underflow 0
		.amdhsa_exception_fp_ieee_inexact 0
		.amdhsa_exception_int_div_zero 0
	.end_amdhsa_kernel

amdhsa.kernels:
  - .agpr_count:     0
    .args:
      - .offset:         0
        .size:           216
        .value_kind:     by_value
      - .offset:         216
        .size:           4
        .value_kind:     hidden_block_count_x
      - .offset:         220
        .size:           4
        .value_kind:     hidden_block_count_y
      - .offset:         224
        .size:           4
        .value_kind:     hidden_block_count_z
      - .offset:         228
        .size:           2
        .value_kind:     hidden_group_size_x
      - .offset:         230
        .size:           2
        .value_kind:     hidden_group_size_y
      - .offset:         232
        .size:           2
        .value_kind:     hidden_group_size_z
      - .offset:         234
        .size:           2
        .value_kind:     hidden_remainder_x
      - .offset:         236
        .size:           2
        .value_kind:     hidden_remainder_y
      - .offset:         238
        .size:           2
        .value_kind:     hidden_remainder_z
      - .offset:         256
        .size:           8
        .value_kind:     hidden_global_offset_x
      - .offset:         264
        .size:           8
        .value_kind:     hidden_global_offset_y
      - .offset:         272
        .size:           8
        .value_kind:     hidden_global_offset_z
      - .offset:         280
        .size:           2
        .value_kind:     hidden_grid_dims
      - .offset:         336
        .size:           4
        .value_kind:     hidden_dynamic_lds_size
    .group_segment_fixed_size: 16384
    .kernarg_segment_align: 8
    .kernarg_segment_size: 472
    .language:       OpenCL C
    .language_version:
      - 2
      - 0
    .max_flat_workgroup_size: 512
    .name:           _ZN2mk3fwdENS_4ArgsE
    .private_segment_fixed_size: 0
    .sgpr_count:     104
    .sgpr_spill_count: 61
    .symbol:         _ZN2mk3fwdENS_4ArgsE.kd
    .uniform_work_group_size: 1
    .uses_dynamic_stack: false
    .vgpr_count:     256
    .vgpr_spill_count: 0
    .wavefront_size: 64
